# chunk-loop state update: the first four fragment pairs are requested 19 VALU instructions earlier (right behind the previous LDS drain)
# baseline (speedup 1.0000x reference)
; __device__ __forceinline__ void unit(const bf16_t* __restrict__ proj, const float* __restrict__ rope, const float* __restrict__ log_decay, const float* __restrict__ gn_g, bf16_t* __restrict__ ymix, ...
;     ...
;         { float s = 0.f;
; #pragma unroll
;           for (int mbv = 0; mbv < 8; ++mbv) s += (yacc[mbv][0] + yacc[mbv][1]) + (yacc[mbv][2] + yacc[mbv][3]);
;           s += __shfl_xor(s, 16); s += __shfl_xor(s, 32);
;           const float mu = s * (1.f / 128.f); float s2 = 0.f;
; #pragma unroll
;           for (int mbv = 0; mbv < 8; ++mbv) { yacc[mbv] = yacc[mbv] - mu; s2 += (yacc[mbv][0] * yacc[mbv][0] + yacc[mbv][1] * yacc[mbv][1]) + (yacc[mbv][2] * yacc[mbv][2] + yacc[mbv][3] * yacc[mbv][3]); }
;           s2 += __shfl_xor(s2, 16); s2 += __shfl_xor(s2, 32);
;           const float rstd = 1.f / sqrtf(s2 * (1.f / 128.f) + GN_EPS);
.LBB0_300:
	v_mov_b32_e32 v116, v144
	v_mov_b32_e32 v117, v112
	v_mov_b32_e32 v118, v145
	v_mov_b32_e32 v119, v113
	v_pk_add_f32 v[116:117], v[116:117], v[118:119]
	v_mov_b32_e32 v118, v146
	v_mov_b32_e32 v119, v114
	v_mov_b32_e32 v120, v147
	v_mov_b32_e32 v121, v115
	v_pk_add_f32 v[118:119], v[118:119], v[120:121]
	v_mov_b32_e32 v120, v140
	v_pk_add_f32 v[116:117], v[116:117], v[118:119]
	v_mov_b32_e32 v118, v141
	v_mov_b32_e32 v119, v142
	v_mov_b32_e32 v121, v143
	v_pk_add_f32 v[118:119], v[118:119], v[120:121]
	v_add_f32_e32 v116, 0, v116
	v_pk_add_f32 v[118:119], v[118:119], v[118:119] op_sel:[0,1] op_sel_hi:[1,0]
	v_add_f32_e32 v116, v116, v117
	v_add_f32_e32 v120, v132, v133
	v_add_f32_e32 v122, v134, v135
	v_mov_b32_e32 v117, v104
	v_mov_b32_e32 v119, v105
	v_mov_b32_e32 v121, v106
	v_mov_b32_e32 v123, v107
	v_pk_add_f32 v[116:117], v[116:117], v[118:119]
	v_pk_add_f32 v[118:119], v[120:121], v[122:123]
	v_mov_b32_e32 v120, v100
	v_pk_add_f32 v[116:117], v[116:117], v[118:119]
	v_mov_b32_e32 v118, v101
	v_mov_b32_e32 v119, v102
	v_mov_b32_e32 v121, v103
	v_pk_add_f32 v[118:119], v[118:119], v[120:121]
	v_pk_add_f32 v[116:117], v[116:117], v[116:117] op_sel:[0,1] op_sel_hi:[1,0]
	v_pk_add_f32 v[118:119], v[118:119], v[118:119] op_sel:[0,1] op_sel_hi:[1,0]
	v_add_f32_e32 v120, v96, v97
	v_add_f32_e32 v122, v98, v99
	v_mov_b32_e32 v117, v108
	v_mov_b32_e32 v119, v109
	v_mov_b32_e32 v121, v110
	v_mov_b32_e32 v123, v111
	v_pk_add_f32 v[116:117], v[116:117], v[118:119]
	v_pk_add_f32 v[118:119], v[120:121], v[122:123]
	v_ashrrev_i32_e32 v187, 31, v186
	v_pk_add_f32 v[116:117], v[116:117], v[118:119]
	v_mov_b32_e32 v185, v177
	v_add_f32_e32 v116, v116, v117
	ds_bpermute_b32 v117, v195, v116
	s_add_i32 s5, s5, 1
	s_add_u32 s60, s60, 0x9000
	s_addc_u32 s61, s61, 0
	s_addk_i32 s84, 0x80
	s_waitcnt lgkmcnt(0)
	v_add_f32_e32 v116, v116, v117
	ds_bpermute_b32 v117, v196, v116
	s_cmp_lg_u32 s60, 0x48000
	s_waitcnt lgkmcnt(0)
	v_add_f32_e32 v116, v116, v117
	v_fmamk_f32 v138, v116, 0xbc000000, v147
	v_fmac_f32_e32 v145, 0xbc000000, v116
	v_fmamk_f32 v131, v116, 0xbc000000, v115
	v_fmac_f32_e32 v113, 0xbc000000, v116
	v_fmamk_f32 v137, v116, 0xbc000000, v146
	v_fmamk_f32 v139, v116, 0xbc000000, v144
	v_mul_f32_e32 v117, v145, v145
	v_mul_f32_e32 v118, v138, v138
	v_fmamk_f32 v136, v116, 0xbc000000, v114
	v_fmamk_f32 v144, v116, 0xbc000000, v112
	v_mul_f32_e32 v112, v113, v113
	v_mul_f32_e32 v114, v131, v131
	v_fmac_f32_e32 v117, v139, v139
	v_fmac_f32_e32 v118, v137, v137
	v_fmac_f32_e32 v112, v144, v144
	v_fmac_f32_e32 v114, v136, v136
	v_add_f32_e32 v117, v117, v118
	v_add_f32_e32 v112, v112, v114
	v_add_f32_e32 v114, v117, v112
	v_fmamk_f32 v112, v116, 0xbc000000, v143
	v_fmac_f32_e32 v141, 0xbc000000, v116
	v_fmamk_f32 v129, v116, 0xbc000000, v142
	v_fmamk_f32 v130, v116, 0xbc000000, v140
	v_mul_f32_e32 v115, v141, v141
	v_mul_f32_e32 v117, v112, v112
	v_fmac_f32_e32 v115, v130, v130
	v_fmac_f32_e32 v117, v129, v129
	v_add_f32_e32 v115, v115, v117
	v_fmamk_f32 v126, v116, 0xbc000000, v135
	v_fmac_f32_e32 v133, 0xbc000000, v116
	v_add_f32_e32 v114, v115, v114
	v_fmamk_f32 v127, v116, 0xbc000000, v134
	v_fmamk_f32 v128, v116, 0xbc000000, v132
	v_mul_f32_e32 v115, v133, v133
	v_mul_f32_e32 v117, v126, v126
	v_fmamk_f32 v124, v116, 0xbc000000, v107
	v_fmac_f32_e32 v105, 0xbc000000, v116
	v_fmac_f32_e32 v115, v128, v128
	v_fmac_f32_e32 v117, v127, v127
	v_fmamk_f32 v125, v116, 0xbc000000, v106
	v_fmamk_f32 v104, v116, 0xbc000000, v104
	v_mul_f32_e32 v106, v105, v105
	v_mul_f32_e32 v107, v124, v124
	v_fmamk_f32 v121, v116, 0xbc000000, v103
	v_fmac_f32_e32 v101, 0xbc000000, v116
	v_add_f32_e32 v115, v115, v117
	v_fmac_f32_e32 v106, v104, v104
	v_fmac_f32_e32 v107, v125, v125
	v_fmamk_f32 v122, v116, 0xbc000000, v102
	v_fmamk_f32 v123, v116, 0xbc000000, v100
	v_mul_f32_e32 v100, v101, v101
	v_mul_f32_e32 v102, v121, v121
	v_fmamk_f32 v118, v116, 0xbc000000, v99
	v_fmac_f32_e32 v97, 0xbc000000, v116
	v_add_f32_e32 v114, v115, v114
	v_add_f32_e32 v106, v106, v107
	v_fmac_f32_e32 v100, v123, v123
	v_fmac_f32_e32 v102, v122, v122
	v_fmamk_f32 v119, v116, 0xbc000000, v98
	v_fmamk_f32 v120, v116, 0xbc000000, v96
	v_mul_f32_e32 v96, v97, v97
	v_mul_f32_e32 v98, v118, v118
	v_add_f32_e32 v106, v106, v114
	v_add_f32_e32 v100, v100, v102
	v_fmac_f32_e32 v96, v120, v120
	v_fmac_f32_e32 v98, v119, v119
	v_add_f32_e32 v100, v100, v106
	v_add_f32_e32 v96, v96, v98
	v_add_f32_e32 v98, v96, v100
	v_fmamk_f32 v96, v116, 0xbc000000, v111
	v_fmac_f32_e32 v109, 0xbc000000, v116
	v_fmamk_f32 v100, v116, 0xbc000000, v110
	v_fmamk_f32 v106, v116, 0xbc000000, v108
	v_mul_f32_e32 v99, v109, v109
	v_mul_f32_e32 v102, v96, v96
	v_fmac_f32_e32 v99, v106, v106
	v_fmac_f32_e32 v102, v100, v100
	v_add_f32_e32 v99, v99, v102
	v_add_f32_e32 v98, v99, v98
	ds_bpermute_b32 v99, v195, v98
	s_waitcnt vmcnt(0)
	v_lshlrev_b32_e32 v110, 16, v191
	v_and_b32_e32 v111, 0xffff0000, v191
	s_waitcnt lgkmcnt(0)
	v_add_f32_e32 v98, v98, v99
	ds_bpermute_b32 v99, v196, v98
	s_waitcnt lgkmcnt(0)
; #define LAS __attribute__((address_space(3)))
; __device__ __forceinline__ float silu_f(float v) { return v * __builtin_amdgcn_rcpf(1.f + __expf(-v)); }
; __device__ __forceinline__ float clamp8(float v) { return __builtin_amdgcn_fmed3f(v, -440.f, 440.f); }
; __device__ __forceinline__ void unit(const bf16_t* __restrict__ proj, const float* __restrict__ rope, const float* __restrict__ log_decay, const float* __restrict__ gn_g, bf16_t* __restrict__ ymix, ...
;     ...
;           const float rstd = 1.f / sqrtf(s2 * (1.f / 128.f) + GN_EPS);
;           unsigned char* op = (unsigned char*)ymix + (size_t)(b * SEQ + tq) * D + 512 + h * 128 + 4 * g;
; #pragma unroll
;           for (int rep4 = 0; rep4 < (RET_PROBE == 4 ? 2 : 1); ++rep4) {
;           if (RET_PROBE == 4) { asm volatile("" : "+v"(op)); asm volatile("" : "+v"(gv[0]), "+v"(gv[1]), "+v"(gv[2]), "+v"(gv[3]), "+v"(gv[4]), "+v"(gv[5]), "+v"(gv[6]), "+v"(gv[7])); }
; #pragma unroll
;           for (int mbv = 0; mbv < 8; ++mbv) {
;               const f32x4 gn = *(const LAS f32x4*)(gnp + 16 * mbv + 4 * g);
;               const float g0 = __uint_as_float(gv[mbv].x << 16), g1 = __uint_as_float(gv[mbv].x & 0xffff0000u), g2 = __uint_as_float(gv[mbv].y << 16), g3 = __uint_as_float(gv[mbv].y & 0xffff0000u);
;               int o = __builtin_amdgcn_cvt_pk_fp8_f32(clamp8(S_H8 * silu_f(g0) * (yacc[mbv][0] * rstd * gn.x)), clamp8(S_H8 * silu_f(g1) * (yacc[mbv][1] * rstd * gn.y)), 0, false);
;               o = __builtin_amdgcn_cvt_pk_fp8_f32(clamp8(S_H8 * silu_f(g2) * (yacc[mbv][2] * rstd * gn.z)), clamp8(S_H8 * silu_f(g3) * (yacc[mbv][3] * rstd * gn.w)), o, true);
;               *(unsigned*)(op + 16 * mbv) = (unsigned)o;
	v_add_f32_e32 v98, v98, v99
	v_fmamk_f32 v98, v98, 0x3c000000, v197
	v_cmp_gt_f32_e32 vcc, s71, v98
	v_mul_f32_e32 v99, 0x4f800000, v98
	s_nop 0
	v_cndmask_b32_e32 v98, v98, v99, vcc
	v_sqrt_f32_e32 v99, v98
	s_nop 0
	v_add_u32_e32 v102, -1, v99
	v_fma_f32 v103, -v102, v99, v98
	v_cmp_ge_f32_e64 s[8:9], 0, v103
	v_add_u32_e32 v103, 1, v99
	s_nop 0
	v_cndmask_b32_e64 v102, v99, v102, s[8:9]
	v_fma_f32 v99, -v103, v99, v98
	v_cmp_lt_f32_e64 s[8:9], 0, v99
	s_nop 1
	v_cndmask_b32_e64 v99, v102, v103, s[8:9]
	v_mul_f32_e32 v102, 0x37800000, v99
	v_cndmask_b32_e32 v99, v99, v102, vcc
	v_cmp_class_f32_e32 vcc, v98, v198
	s_nop 1
	v_cndmask_b32_e32 v98, v99, v98, vcc
	v_div_scale_f32 v99, s[8:9], v98, v98, 1.0
	v_rcp_f32_e32 v102, v99
	s_nop 0
	v_fma_f32 v103, -v99, v102, 1.0
	v_fmac_f32_e32 v102, v103, v102
	v_div_scale_f32 v103, vcc, 1.0, v98, 1.0
	v_mul_f32_e32 v107, v103, v102
	v_fma_f32 v108, -v99, v107, v103
	v_fmac_f32_e32 v107, v108, v102
	v_fma_f32 v99, -v99, v107, v103
	v_div_fmas_f32 v99, v99, v102, v107
	v_lshlrev_b32_e32 v102, 16, v190
	v_mul_f32_e32 v132, 0xbfb8aa3b, v102
	v_exp_f32_e32 v132, v132
	v_lshl_add_u32 v108, v184, 2, v206
	ds_read_b128 v[114:117], v108
	v_div_fixup_f32 v107, v99, v98, 1.0
	v_add_f32_e32 v132, 1.0, v132
	v_rcp_f32_e32 v132, v132
	v_and_b32_e32 v103, 0xffff0000, v190
	v_lshlrev_b64 v[98:99], 10, v[186:187]
	v_lshl_add_u64 v[98:99], v[182:183], 0, v[98:99]
	v_mul_f32_e32 v102, v132, v102
	v_mul_f32_e32 v132, v139, v107
	v_mul_f32_e32 v102, 0x41800000, v102
	s_waitcnt lgkmcnt(0)
	v_mul_f32_e32 v114, v114, v132
	v_mul_f32_e32 v102, v102, v114
	v_mul_f32_e32 v114, 0xbfb8aa3b, v103
	v_exp_f32_e32 v114, v114
	v_med3_f32 v102, v102, s72, v200
	v_lshl_add_u64 v[98:99], v[98:99], 0, v[184:185]
	v_mul_f32_e32 v113, v113, v107
	v_add_f32_e32 v114, 1.0, v114
	v_rcp_f32_e32 v114, v114
	v_mul_f32_e32 v104, v104, v107
	v_mul_f32_e32 v101, v101, v107
	v_mul_f32_e32 v97, v97, v107
	v_mul_f32_e32 v103, v114, v103
	v_mul_f32_e32 v114, v145, v107
	v_mul_f32_e32 v103, 0x41800000, v103
	v_mul_f32_e32 v114, v115, v114
	v_mul_f32_e32 v103, v103, v114
	v_med3_f32 v103, v103, s72, v200
	v_mov_b32_e32 v114, v177
	v_cvt_pk_fp8_f32 v114, v102, v103
	v_mul_f32_e32 v102, 0xbfb8aa3b, v110
	v_exp_f32_e32 v102, v102
	v_mul_f32_e32 v103, v137, v107
	v_mul_f32_e32 v103, v116, v103
	v_mul_f32_e32 v106, v106, v107
	v_add_f32_e32 v102, 1.0, v102
	v_rcp_f32_e32 v102, v102
	v_mul_f32_e32 v100, v100, v107
	v_mul_f32_e32 v96, v96, v107
	v_mul_f32_e32 v102, v102, v110
	v_mul_f32_e32 v102, 0x41800000, v102
	v_mul_f32_e32 v102, v102, v103
	v_mul_f32_e32 v103, 0xbfb8aa3b, v111
	v_exp_f32_e32 v103, v103
	v_mul_f32_e32 v110, v138, v107
	v_mul_f32_e32 v110, v117, v110
	v_med3_f32 v102, v102, s72, v200
	v_add_f32_e32 v103, 1.0, v103
	v_rcp_f32_e32 v103, v103
	s_nop 0
	v_mul_f32_e32 v103, v103, v111
	v_mul_f32_e32 v103, 0x41800000, v103
	v_mul_f32_e32 v103, v103, v110
	v_med3_f32 v103, v103, s72, v200
	v_cvt_pk_fp8_f32 v114, v102, v103 op_sel:[0,0,1]
	v_lshlrev_b32_e32 v102, 16, v188
	v_mul_f32_e32 v132, 0xbfb8aa3b, v102
	v_exp_f32_e32 v132, v132
	global_store_dword v[98:99], v114, off offset:512
	ds_read_b128 v[114:117], v108 offset:64
	v_and_b32_e32 v103, 0xffff0000, v188
	v_add_f32_e32 v132, 1.0, v132
	v_rcp_f32_e32 v132, v132
	v_lshlrev_b32_e32 v110, 16, v189
	s_waitcnt lgkmcnt(0)
	v_mul_f32_e32 v113, v115, v113
	v_and_b32_e32 v111, 0xffff0000, v189
	v_mul_f32_e32 v102, v132, v102
	v_mul_f32_e32 v132, v144, v107
	v_mul_f32_e32 v102, 0x41800000, v102
	v_mul_f32_e32 v114, v114, v132
	v_mul_f32_e32 v102, v102, v114
	v_mul_f32_e32 v114, 0xbfb8aa3b, v103
	v_exp_f32_e32 v114, v114
	v_med3_f32 v102, v102, s72, v200
	v_add_f32_e32 v114, 1.0, v114
	v_rcp_f32_e32 v114, v114
	s_nop 0
	v_mul_f32_e32 v103, v114, v103
	v_mul_f32_e32 v103, 0x41800000, v103
	v_mul_f32_e32 v103, v103, v113
	v_med3_f32 v103, v103, s72, v200
	v_mov_b32_e32 v113, v177
	v_cvt_pk_fp8_f32 v113, v102, v103
	v_mul_f32_e32 v102, 0xbfb8aa3b, v110
	v_exp_f32_e32 v102, v102
	v_mul_f32_e32 v103, v136, v107
	v_mul_f32_e32 v103, v116, v103
	v_add_f32_e32 v102, 1.0, v102
	v_rcp_f32_e32 v102, v102
	s_nop 0
	v_mul_f32_e32 v102, v102, v110
	v_mul_f32_e32 v102, 0x41800000, v102
	v_mul_f32_e32 v102, v102, v103
	v_mul_f32_e32 v103, 0xbfb8aa3b, v111
	v_exp_f32_e32 v103, v103
	v_mul_f32_e32 v110, v131, v107
	v_mul_f32_e32 v110, v117, v110
	v_med3_f32 v102, v102, s72, v200
	v_add_f32_e32 v103, 1.0, v103
	v_rcp_f32_e32 v103, v103
	ds_read_b128 v[114:117], v108 offset:128
	v_mul_f32_e32 v103, v103, v111
	v_mul_f32_e32 v103, 0x41800000, v103
	v_mul_f32_e32 v103, v103, v110
	v_med3_f32 v103, v103, s72, v200
	v_cvt_pk_fp8_f32 v113, v102, v103 op_sel:[0,0,1]
	v_lshlrev_b32_e32 v102, 16, v172
	v_and_b32_e32 v103, 0xffff0000, v172
	v_lshlrev_b32_e32 v110, 16, v173
	global_store_dword v[98:99], v113, off offset:528
	v_mul_f32_e32 v113, 0xbfb8aa3b, v102
	v_exp_f32_e32 v113, v113
	v_and_b32_e32 v111, 0xffff0000, v173
	v_add_f32_e32 v113, 1.0, v113
	v_rcp_f32_e32 v113, v113
	s_nop 0
	v_mul_f32_e32 v102, v113, v102
	v_mul_f32_e32 v113, v130, v107
	v_mul_f32_e32 v102, 0x41800000, v102
	s_waitcnt lgkmcnt(0)
; #define LAS __attribute__((address_space(3)))
; __device__ __forceinline__ float silu_f(float v) { return v * __builtin_amdgcn_rcpf(1.f + __expf(-v)); }
; __device__ __forceinline__ float clamp8(float v) { return __builtin_amdgcn_fmed3f(v, -440.f, 440.f); }
; __device__ __forceinline__ void unit(const bf16_t* __restrict__ proj, const float* __restrict__ rope, const float* __restrict__ log_decay, const float* __restrict__ gn_g, bf16_t* __restrict__ ymix, ...
;     ...
; #pragma unroll
;           for (int mbv = 0; mbv < 8; ++mbv) {
;               const f32x4 gn = *(const LAS f32x4*)(gnp + 16 * mbv + 4 * g);
;               const float g0 = __uint_as_float(gv[mbv].x << 16), g1 = __uint_as_float(gv[mbv].x & 0xffff0000u), g2 = __uint_as_float(gv[mbv].y << 16), g3 = __uint_as_float(gv[mbv].y & 0xffff0000u);
;               int o = __builtin_amdgcn_cvt_pk_fp8_f32(clamp8(S_H8 * silu_f(g0) * (yacc[mbv][0] * rstd * gn.x)), clamp8(S_H8 * silu_f(g1) * (yacc[mbv][1] * rstd * gn.y)), 0, false);
;               o = __builtin_amdgcn_cvt_pk_fp8_f32(clamp8(S_H8 * silu_f(g2) * (yacc[mbv][2] * rstd * gn.z)), clamp8(S_H8 * silu_f(g3) * (yacc[mbv][3] * rstd * gn.w)), o, true);
;               *(unsigned*)(op + 16 * mbv) = (unsigned)o;
;           } } }
	v_mul_f32_e32 v113, v114, v113
	v_mul_f32_e32 v102, v102, v113
	v_mul_f32_e32 v113, 0xbfb8aa3b, v103
	v_exp_f32_e32 v113, v113
	v_med3_f32 v102, v102, s72, v200
	v_lshlrev_b32_e32 v114, 16, v171
	v_add_f32_e32 v113, 1.0, v113
	v_rcp_f32_e32 v113, v113
	s_nop 0
	v_mul_f32_e32 v103, v113, v103
	v_mul_f32_e32 v113, v141, v107
	v_mul_f32_e32 v103, 0x41800000, v103
	v_mul_f32_e32 v113, v115, v113
	v_mul_f32_e32 v103, v103, v113
	v_med3_f32 v103, v103, s72, v200
	v_mov_b32_e32 v113, v177
	v_cvt_pk_fp8_f32 v113, v102, v103
	v_mul_f32_e32 v102, 0xbfb8aa3b, v110
	v_exp_f32_e32 v102, v102
	v_mul_f32_e32 v103, v129, v107
	v_mul_f32_e32 v103, v116, v103
	v_and_b32_e32 v115, 0xffff0000, v171
	v_add_f32_e32 v102, 1.0, v102
	v_rcp_f32_e32 v102, v102
	s_nop 0
	v_mul_f32_e32 v102, v102, v110
	v_mul_f32_e32 v102, 0x41800000, v102
	v_mul_f32_e32 v102, v102, v103
	v_mul_f32_e32 v103, 0xbfb8aa3b, v111
	v_exp_f32_e32 v103, v103
	v_mul_f32_e32 v110, v112, v107
	v_mul_f32_e32 v110, v117, v110
	v_med3_f32 v102, v102, s72, v200
	v_add_f32_e32 v103, 1.0, v103
	v_rcp_f32_e32 v103, v103
	s_nop 0
	v_mul_f32_e32 v103, v103, v111
	v_mul_f32_e32 v103, 0x41800000, v103
	v_mul_f32_e32 v103, v103, v110
	v_med3_f32 v103, v103, s72, v200
	v_cvt_pk_fp8_f32 v113, v102, v103 op_sel:[0,0,1]
	v_lshlrev_b32_e32 v102, 16, v170
	v_mul_f32_e32 v116, 0xbfb8aa3b, v102
	v_exp_f32_e32 v116, v116
	global_store_dword v[98:99], v113, off offset:544
	ds_read_b128 v[110:113], v108 offset:192
	v_and_b32_e32 v103, 0xffff0000, v170
	v_add_f32_e32 v116, 1.0, v116
	v_rcp_f32_e32 v116, v116
	s_nop 0
	v_mul_f32_e32 v102, v116, v102
	v_mul_f32_e32 v116, v128, v107
	v_mul_f32_e32 v102, 0x41800000, v102
	s_waitcnt lgkmcnt(0)
	v_mul_f32_e32 v110, v110, v116
	v_mul_f32_e32 v102, v102, v110
	v_mul_f32_e32 v110, 0xbfb8aa3b, v103
	v_exp_f32_e32 v110, v110
	v_med3_f32 v102, v102, s72, v200
	v_add_f32_e32 v110, 1.0, v110
	v_rcp_f32_e32 v110, v110
	s_nop 0
	v_mul_f32_e32 v103, v110, v103
	v_mul_f32_e32 v110, v133, v107
	v_mul_f32_e32 v103, 0x41800000, v103
	v_mul_f32_e32 v110, v111, v110
	v_mul_f32_e32 v103, v103, v110
	v_med3_f32 v103, v103, s72, v200
	v_mov_b32_e32 v110, v177
	v_cvt_pk_fp8_f32 v110, v102, v103
	v_mul_f32_e32 v102, 0xbfb8aa3b, v114
	v_exp_f32_e32 v102, v102
	v_mul_f32_e32 v103, v127, v107
	v_mul_f32_e32 v103, v112, v103
	v_mul_f32_e32 v111, v126, v107
	v_add_f32_e32 v102, 1.0, v102
	v_rcp_f32_e32 v102, v102
	v_mul_f32_e32 v111, v113, v111
	v_mul_f32_e32 v102, v102, v114
	v_mul_f32_e32 v102, 0x41800000, v102
	v_mul_f32_e32 v102, v102, v103
	v_mul_f32_e32 v103, 0xbfb8aa3b, v115
	v_exp_f32_e32 v103, v103
	v_med3_f32 v102, v102, s72, v200
	v_lshlrev_b32_e32 v114, 16, v169
	v_add_f32_e32 v103, 1.0, v103
	v_rcp_f32_e32 v103, v103
	s_nop 0
	v_mul_f32_e32 v103, v103, v115
	v_mul_f32_e32 v103, 0x41800000, v103
	v_mul_f32_e32 v103, v103, v111
	v_med3_f32 v103, v103, s72, v200
	v_cvt_pk_fp8_f32 v110, v102, v103 op_sel:[0,0,1]
	v_lshlrev_b32_e32 v102, 16, v168
	v_mul_f32_e32 v116, 0xbfb8aa3b, v102
	v_exp_f32_e32 v116, v116
	global_store_dword v[98:99], v110, off offset:560
	ds_read_b128 v[110:113], v108 offset:256
	v_and_b32_e32 v103, 0xffff0000, v168
	v_add_f32_e32 v116, 1.0, v116
	v_rcp_f32_e32 v116, v116
	v_and_b32_e32 v115, 0xffff0000, v169
	s_waitcnt lgkmcnt(0)
	v_mul_f32_e32 v104, v110, v104
	v_lshlrev_b32_e32 v110, 16, v156
	v_mul_f32_e32 v102, v116, v102
	v_mul_f32_e32 v102, 0x41800000, v102
	v_mul_f32_e32 v102, v102, v104
	v_mul_f32_e32 v104, 0xbfb8aa3b, v103
	v_exp_f32_e32 v104, v104
	v_med3_f32 v102, v102, s72, v200
	v_add_f32_e32 v104, 1.0, v104
	v_rcp_f32_e32 v104, v104
	s_nop 0
	v_mul_f32_e32 v103, v104, v103
	v_mul_f32_e32 v104, v105, v107
	v_mul_f32_e32 v103, 0x41800000, v103
	v_mul_f32_e32 v104, v111, v104
	v_mul_f32_e32 v103, v103, v104
	v_med3_f32 v103, v103, s72, v200
	v_mov_b32_e32 v104, v177
	v_cvt_pk_fp8_f32 v104, v102, v103
	v_mul_f32_e32 v102, 0xbfb8aa3b, v114
	v_exp_f32_e32 v102, v102
	v_mul_f32_e32 v103, v125, v107
	v_mul_f32_e32 v103, v112, v103
	v_mul_f32_e32 v105, v124, v107
	v_add_f32_e32 v102, 1.0, v102
	v_rcp_f32_e32 v102, v102
	v_mul_f32_e32 v105, v113, v105
	v_and_b32_e32 v111, 0xffff0000, v156
	v_lshlrev_b32_e32 v112, 16, v157
	v_mul_f32_e32 v102, v102, v114
	v_mul_f32_e32 v102, 0x41800000, v102
	v_mul_f32_e32 v102, v102, v103
	v_mul_f32_e32 v103, 0xbfb8aa3b, v115
	v_exp_f32_e32 v103, v103
	v_mul_f32_e32 v114, 0xbfb8aa3b, v110
	v_med3_f32 v102, v102, s72, v200
	v_exp_f32_e32 v114, v114
	v_add_f32_e32 v103, 1.0, v103
	v_rcp_f32_e32 v103, v103
	v_and_b32_e32 v113, 0xffff0000, v157
	v_add_f32_e32 v114, 1.0, v114
	v_rcp_f32_e32 v114, v114
	v_mul_f32_e32 v103, v103, v115
	v_mul_f32_e32 v103, 0x41800000, v103
	v_mul_f32_e32 v103, v103, v105
	v_med3_f32 v103, v103, s72, v200
	v_cvt_pk_fp8_f32 v104, v102, v103 op_sel:[0,0,1]
	v_mul_f32_e32 v110, v114, v110
	v_mul_f32_e32 v114, v123, v107
	v_mul_f32_e32 v110, 0x41800000, v110
	global_store_dword v[98:99], v104, off offset:576
	ds_read_b128 v[102:105], v108 offset:320
	s_waitcnt lgkmcnt(0)
; #define LAS __attribute__((address_space(3)))
; __device__ __forceinline__ float silu_f(float v) { return v * __builtin_amdgcn_rcpf(1.f + __expf(-v)); }
; __device__ __forceinline__ float clamp8(float v) { return __builtin_amdgcn_fmed3f(v, -440.f, 440.f); }
; __device__ __forceinline__ bf16x8 pack8(const float (&f)[8]) { u32x4 u; u.x = cvtpk(f[0], f[1]); u.y = cvtpk(f[2], f[3]); u.z = cvtpk(f[4], f[5]); u.w = cvtpk(f[6], f[7]); return __builtin_bit_cast(bf16x8, u); }
; template <bool FWD> __device__ __forceinline__ void state_update_1(LAS unsigned char* lds, f32x4 (&racc)[8], float l2, int w, int g, unsigned qp, unsigned p) {
;     const float dec = __builtin_amdgcn_exp2f(128.f * l2);
;     bf16x8 vs[4];
; #pragma unroll
;     for (int ks = 0; ks < 4; ++ks) {
;         float f[8]; unpack8(trfrag(lds + LV, 32 * ks + 4 * g, 32 * ks + 16 + 4 * g, w, qp, p), f);
; #pragma unroll
;         for (int e = 0; e < 8; ++e) { const int key = 32 * ks + 16 * (e >> 2) + 4 * g + (e & 3); f[e] *= __builtin_amdgcn_exp2f((FWD ? (float)(127 - key) : (float)key) * l2); }
;         vs[ks] = pack8(f);
; __device__ __forceinline__ void unit(const bf16_t* __restrict__ proj, const float* __restrict__ rope, const float* __restrict__ log_decay, const float* __restrict__ gn_g, bf16_t* __restrict__ ymix, ...
;     ...
; #pragma unroll
;           for (int mbv = 0; mbv < 8; ++mbv) {
;               const f32x4 gn = *(const LAS f32x4*)(gnp + 16 * mbv + 4 * g);
;               const float g0 = __uint_as_float(gv[mbv].x << 16), g1 = __uint_as_float(gv[mbv].x & 0xffff0000u), g2 = __uint_as_float(gv[mbv].y << 16), g3 = __uint_as_float(gv[mbv].y & 0xffff0000u);
;               int o = __builtin_amdgcn_cvt_pk_fp8_f32(clamp8(S_H8 * silu_f(g0) * (yacc[mbv][0] * rstd * gn.x)), clamp8(S_H8 * silu_f(g1) * (yacc[mbv][1] * rstd * gn.y)), 0, false);
;               o = __builtin_amdgcn_cvt_pk_fp8_f32(clamp8(S_H8 * silu_f(g2) * (yacc[mbv][2] * rstd * gn.z)), clamp8(S_H8 * silu_f(g3) * (yacc[mbv][3] * rstd * gn.w)), o, true);
;               *(unsigned*)(op + 16 * mbv) = (unsigned)o;
;           } } }
	v_mul_f32_e32 v102, v102, v114
	v_mul_f32_e32 v102, v110, v102
	v_mul_f32_e32 v110, 0xbfb8aa3b, v111
	v_exp_f32_e32 v110, v110
	v_mul_f32_e32 v101, v103, v101
	v_med3_f32 v102, v102, s72, v200
	v_mov_b32_e32 v103, v177
	v_add_f32_e32 v110, 1.0, v110
	v_rcp_f32_e32 v110, v110
	s_nop 0
	v_mul_f32_e32 v110, v110, v111
	v_mul_f32_e32 v110, 0x41800000, v110
	v_mul_f32_e32 v101, v110, v101
	v_med3_f32 v101, v101, s72, v200
	v_cvt_pk_fp8_f32 v103, v102, v101
	v_mul_f32_e32 v101, 0xbfb8aa3b, v112
	v_exp_f32_e32 v101, v101
	v_mul_f32_e32 v102, v122, v107
	v_mul_f32_e32 v102, v104, v102
	v_mul_f32_e32 v104, v121, v107
	v_add_f32_e32 v101, 1.0, v101
	v_rcp_f32_e32 v101, v101
	v_mul_f32_e32 v104, v105, v104
	v_and_b32_e32 v110, 0xffff0000, v154
	v_lshlrev_b32_e32 v111, 16, v155
	v_mul_f32_e32 v101, v101, v112
	v_mul_f32_e32 v101, 0x41800000, v101
	v_mul_f32_e32 v101, v101, v102
	v_mul_f32_e32 v102, 0xbfb8aa3b, v113
	v_exp_f32_e32 v102, v102
	v_med3_f32 v101, v101, s72, v200
	v_and_b32_e32 v112, 0xffff0000, v155
	v_add_f32_e32 v102, 1.0, v102
	v_rcp_f32_e32 v102, v102
	s_nop 0
	v_mul_f32_e32 v102, v102, v113
	v_mul_f32_e32 v102, 0x41800000, v102
	v_mul_f32_e32 v102, v102, v104
	v_med3_f32 v102, v102, s72, v200
	v_cvt_pk_fp8_f32 v103, v101, v102 op_sel:[0,0,1]
	v_lshlrev_b32_e32 v101, 16, v154
	v_mul_f32_e32 v113, 0xbfb8aa3b, v101
	v_exp_f32_e32 v113, v113
	global_store_dword v[98:99], v103, off offset:592
	ds_read_b128 v[102:105], v108 offset:384
	v_add_f32_e32 v113, 1.0, v113
	v_rcp_f32_e32 v113, v113
	s_waitcnt lgkmcnt(0)
	v_mul_f32_e32 v97, v97, v103
	v_mul_f32_e32 v103, v118, v107
	v_mul_f32_e32 v101, v113, v101
	v_mul_f32_e32 v113, v120, v107
	v_mul_f32_e32 v101, 0x41800000, v101
	v_mul_f32_e32 v102, v113, v102
	v_mul_f32_e32 v101, v101, v102
	v_mul_f32_e32 v102, 0xbfb8aa3b, v110
	v_exp_f32_e32 v102, v102
	v_med3_f32 v101, v101, s72, v200
	v_mul_f32_e32 v103, v103, v105
	v_xor_b32_e32 v113, 31, v184
	v_add_f32_e32 v102, 1.0, v102
	v_rcp_f32_e32 v102, v102
	v_cvt_f32_ubyte0_e32 v113, v113
	v_mul_f32_e32 v113, v204, v113
	v_mul_f32_e32 v102, v102, v110
	v_mul_f32_e32 v102, 0x41800000, v102
	v_mul_f32_e32 v97, v102, v97
	v_med3_f32 v97, v97, s72, v200
	v_mov_b32_e32 v102, v177
	v_cvt_pk_fp8_f32 v102, v101, v97
	v_mul_f32_e32 v97, 0xbfb8aa3b, v111
	v_exp_f32_e32 v97, v97
	v_mul_f32_e32 v101, v119, v107
	v_mul_f32_e32 v101, v101, v104
	v_and_b32_e32 v110, 0xffff0000, v153
	v_add_f32_e32 v97, 1.0, v97
	v_rcp_f32_e32 v97, v97
	s_nop 0
	v_mul_f32_e32 v97, v97, v111
	v_mul_f32_e32 v97, 0x41800000, v97
	v_mul_f32_e32 v97, v97, v101
	v_mul_f32_e32 v101, 0xbfb8aa3b, v112
	v_exp_f32_e32 v101, v101
	v_med3_f32 v97, v97, s72, v200
	v_add_f32_e32 v101, 1.0, v101
	v_rcp_f32_e32 v101, v101
	s_nop 0
	v_mul_f32_e32 v101, v101, v112
	v_mul_f32_e32 v101, 0x41800000, v101
	v_mul_f32_e32 v101, v101, v103
	v_med3_f32 v101, v101, s72, v200
	v_cvt_pk_fp8_f32 v102, v97, v101 op_sel:[0,0,1]
	v_lshlrev_b32_e32 v97, 16, v152
	v_mul_f32_e32 v111, 0xbfb8aa3b, v97
	v_exp_f32_e32 v111, v111
	global_store_dword v[98:99], v102, off offset:608
	ds_read_b128 v[102:105], v108 offset:448
	v_and_b32_e32 v101, 0xffff0000, v152
	v_add_f32_e32 v111, 1.0, v111
	v_rcp_f32_e32 v111, v111
	v_lshlrev_b32_e32 v108, 16, v153
	s_waitcnt lgkmcnt(0)
	v_mul_f32_e32 v102, v106, v102
	v_mul_f32_e32 v100, v100, v104
	v_mul_f32_e32 v97, v111, v97
	v_mul_f32_e32 v97, 0x41800000, v97
	v_mul_f32_e32 v97, v97, v102
	v_mul_f32_e32 v102, 0xbfb8aa3b, v101
	v_exp_f32_e32 v102, v102
	v_med3_f32 v97, v97, s72, v200
	v_mul_f32_e32 v96, v96, v105
	v_mul_f32_e32 v112, 0x43000000, v204
	v_add_f32_e32 v102, 1.0, v102
	v_rcp_f32_e32 v102, v102
	v_exp_f32_e32 v112, v112
	v_mul_f32_e32 v101, v102, v101
	v_mul_f32_e32 v102, v109, v107
	v_mul_f32_e32 v101, 0x41800000, v101
	v_mul_f32_e32 v102, v102, v103
	v_mul_f32_e32 v101, v101, v102
	v_med3_f32 v101, v101, s72, v200
	v_mov_b32_e32 v102, v177
	v_cvt_pk_fp8_f32 v102, v97, v101
	v_mul_f32_e32 v97, 0xbfb8aa3b, v108
	v_exp_f32_e32 v97, v97
	v_sub_u32_e32 v101, 0x7e, v184
	v_cvt_f32_ubyte0_e32 v101, v101
	v_mul_f32_e32 v101, v204, v101
	v_add_f32_e32 v97, 1.0, v97
	v_rcp_f32_e32 v97, v97
	v_exp_f32_e32 v101, v101
	v_xor_b32_e32 v109, 63, v184
	v_cvt_f32_ubyte0_e32 v109, v109
	v_mul_f32_e32 v97, v97, v108
	v_mul_f32_e32 v97, 0x41800000, v97
	v_mul_f32_e32 v97, v97, v100
	v_mul_f32_e32 v100, 0xbfb8aa3b, v110
	v_exp_f32_e32 v100, v100
	v_med3_f32 v97, v97, s72, v200
	v_mul_f32_e32 v109, v204, v109
	v_add_f32_e32 v100, 1.0, v100
	v_rcp_f32_e32 v100, v100
	s_nop 0
	v_mul_f32_e32 v100, v100, v110
	v_mul_f32_e32 v100, 0x41800000, v100
	v_mul_f32_e32 v96, v100, v96
	v_med3_f32 v96, v96, s72, v200
	v_cvt_pk_fp8_f32 v102, v97, v96 op_sel:[0,0,1]
	v_add_u32_e32 v96, s77, v208
	v_add3_u32 v108, v96, v207, v209
	v_xor_b32_e32 v100, 0x7f, v184
	global_store_dword v[98:99], v102, off offset:624
	ds_read_b64_tr_b16 v[96:97], v108 offset:36864
	ds_read_b64_tr_b16 v[98:99], v108 offset:41472
	v_cvt_f32_ubyte0_e32 v100, v100
	v_mul_f32_e32 v100, v204, v100
	v_exp_f32_e32 v100, v100
	s_waitcnt lgkmcnt(1)
	v_lshlrev_b32_e32 v102, 16, v96
	v_and_b32_e32 v103, 0xffff0000, v96
	v_sub_u32_e32 v96, 0x7d, v184
	v_cvt_f32_ubyte0_e32 v96, v96
	v_mul_f32_e32 v96, v204, v96
	v_pk_mul_f32 v[100:101], v[100:101], v[102:103]
	v_exp_f32_e32 v102, v96
	v_sub_u32_e32 v96, 0x7c, v184
	v_cvt_f32_ubyte0_e32 v96, v96
	v_mul_f32_e32 v96, v204, v96
	v_exp_f32_e32 v103, v96
	v_lshlrev_b32_e32 v96, 16, v97
	v_and_b32_e32 v97, 0xffff0000, v97
	s_waitcnt lgkmcnt(0)
; __device__ __forceinline__ bf16x8 pack8(const float (&f)[8]) { u32x4 u; u.x = cvtpk(f[0], f[1]); u.y = cvtpk(f[2], f[3]); u.z = cvtpk(f[4], f[5]); u.w = cvtpk(f[6], f[7]); return __builtin_bit_cast(bf16x8, u); }
; template <bool FWD> __device__ __forceinline__ void state_update_1(LAS unsigned char* lds, f32x4 (&racc)[8], float l2, int w, int g, unsigned qp, unsigned p) {
;     ...
;     for (int ks = 0; ks < 4; ++ks) {
;         float f[8]; unpack8(trfrag(lds + LV, 32 * ks + 4 * g, 32 * ks + 16 + 4 * g, w, qp, p), f);
; #pragma unroll
;         for (int e = 0; e < 8; ++e) { const int key = 32 * ks + 16 * (e >> 2) + 4 * g + (e & 3); f[e] *= __builtin_amdgcn_exp2f((FWD ? (float)(127 - key) : (float)key) * l2); }
;         vs[ks] = pack8(f);
;     }
	v_lshlrev_b32_e32 v104, 16, v98
	v_pk_mul_f32 v[102:103], v[102:103], v[96:97]
	v_xor_b32_e32 v96, 0x6f, v184
	v_sub_u32_e32 v97, 0x6e, v184
	v_cvt_f32_ubyte0_e32 v96, v96
	v_cvt_f32_ubyte0_e32 v97, v97
	v_mul_f32_e32 v96, v204, v96
	v_mul_f32_e32 v97, v204, v97
	v_exp_f32_e32 v96, v96
	v_exp_f32_e32 v97, v97
	v_and_b32_e32 v105, 0xffff0000, v98
	v_lshlrev_b32_e32 v98, 16, v99
	v_and_b32_e32 v99, 0xffff0000, v99
	v_pk_mul_f32 v[104:105], v[96:97], v[104:105]
	v_sub_u32_e32 v96, 0x6d, v184
	v_sub_u32_e32 v97, 0x6c, v184
	v_cvt_f32_ubyte0_e32 v96, v96
	v_cvt_f32_ubyte0_e32 v97, v97
	v_mul_f32_e32 v96, v204, v96
	v_mul_f32_e32 v97, v204, v97
	v_exp_f32_e32 v96, v96
	v_exp_f32_e32 v97, v97
	s_nop 0
	v_pk_mul_f32 v[106:107], v[96:97], v[98:99]
	v_cvt_pk_bf16_f32 v96, v100, v101
	v_cvt_pk_bf16_f32 v97, v102, v103
	v_cvt_pk_bf16_f32 v98, v104, v105
	ds_read_b64_tr_b16 v[100:101], v108 offset:46080
	ds_read_b64_tr_b16 v[102:103], v108 offset:50688
	v_xor_b32_e32 v104, 0x5f, v184
	v_sub_u32_e32 v105, 0x5e, v184
	v_cvt_f32_ubyte0_e32 v104, v104
	v_cvt_f32_ubyte0_e32 v105, v105
	v_mul_f32_e32 v104, v204, v104
	v_mul_f32_e32 v105, v204, v105
	v_exp_f32_e32 v104, v104
	v_exp_f32_e32 v105, v105
	v_cvt_pk_bf16_f32 v99, v106, v107
	s_waitcnt lgkmcnt(1)
	v_lshlrev_b32_e32 v106, 16, v100
	v_and_b32_e32 v107, 0xffff0000, v100
	v_sub_u32_e32 v100, 0x5d, v184
	v_cvt_f32_ubyte0_e32 v100, v100
	v_mul_f32_e32 v100, v204, v100
	v_pk_mul_f32 v[104:105], v[104:105], v[106:107]
	v_exp_f32_e32 v106, v100
	v_sub_u32_e32 v100, 0x5c, v184
	v_cvt_f32_ubyte0_e32 v100, v100
	v_mul_f32_e32 v100, v204, v100
	v_exp_f32_e32 v107, v100
	v_lshlrev_b32_e32 v100, 16, v101
	v_and_b32_e32 v101, 0xffff0000, v101
	s_waitcnt lgkmcnt(0)
	v_lshlrev_b32_e32 v110, 16, v102
	v_pk_mul_f32 v[106:107], v[106:107], v[100:101]
	v_xor_b32_e32 v100, 0x4f, v184
	v_sub_u32_e32 v101, 0x4e, v184
	v_cvt_f32_ubyte0_e32 v100, v100
	v_cvt_f32_ubyte0_e32 v101, v101
	v_mul_f32_e32 v100, v204, v100
	v_mul_f32_e32 v101, v204, v101
	v_exp_f32_e32 v100, v100
	v_exp_f32_e32 v101, v101
	v_and_b32_e32 v111, 0xffff0000, v102
	v_lshlrev_b32_e32 v102, 16, v103
	v_and_b32_e32 v103, 0xffff0000, v103
	v_pk_mul_f32 v[110:111], v[100:101], v[110:111]
	v_sub_u32_e32 v100, 0x4d, v184
	v_sub_u32_e32 v101, 0x4c, v184
	v_cvt_f32_ubyte0_e32 v100, v100
	v_cvt_f32_ubyte0_e32 v101, v101
	v_mul_f32_e32 v100, v204, v100
	v_mul_f32_e32 v101, v204, v101
	v_exp_f32_e32 v100, v100
	v_exp_f32_e32 v101, v101
	s_nop 0
	v_pk_mul_f32 v[114:115], v[100:101], v[102:103]
	v_cvt_pk_bf16_f32 v100, v104, v105
	v_cvt_pk_bf16_f32 v101, v106, v107
	v_cvt_pk_bf16_f32 v102, v110, v111
	ds_read_b64_tr_b16 v[104:105], v108 offset:55296
	ds_read_b64_tr_b16 v[106:107], v108 offset:59904
	v_exp_f32_e32 v110, v109
	v_sub_u32_e32 v109, 62, v184
	v_cvt_f32_ubyte0_e32 v109, v109
	v_mul_f32_e32 v109, v204, v109
	v_exp_f32_e32 v111, v109
	v_cvt_pk_bf16_f32 v103, v114, v115
	s_waitcnt lgkmcnt(1)
	v_lshlrev_b32_e32 v114, 16, v104
	v_and_b32_e32 v115, 0xffff0000, v104
	v_sub_u32_e32 v104, 61, v184
	v_cvt_f32_ubyte0_e32 v104, v104
	v_mul_f32_e32 v104, v204, v104
	v_pk_mul_f32 v[110:111], v[110:111], v[114:115]
	v_exp_f32_e32 v114, v104
	v_sub_u32_e32 v104, 60, v184
	v_cvt_f32_ubyte0_e32 v104, v104
	v_mul_f32_e32 v104, v204, v104
	v_exp_f32_e32 v115, v104
	v_lshlrev_b32_e32 v104, 16, v105
	v_and_b32_e32 v105, 0xffff0000, v105
	s_waitcnt lgkmcnt(0)
	v_lshlrev_b32_e32 v116, 16, v106
	v_pk_mul_f32 v[114:115], v[114:115], v[104:105]
	v_xor_b32_e32 v104, 47, v184
	v_sub_u32_e32 v105, 46, v184
	v_cvt_f32_ubyte0_e32 v104, v104
	v_cvt_f32_ubyte0_e32 v105, v105
	v_mul_f32_e32 v104, v204, v104
	v_mul_f32_e32 v105, v204, v105
	v_exp_f32_e32 v104, v104
	v_exp_f32_e32 v105, v105
	v_and_b32_e32 v117, 0xffff0000, v106
	v_lshlrev_b32_e32 v106, 16, v107
	v_and_b32_e32 v107, 0xffff0000, v107
	v_pk_mul_f32 v[116:117], v[104:105], v[116:117]
	v_sub_u32_e32 v104, 45, v184
	v_sub_u32_e32 v105, 44, v184
	v_cvt_f32_ubyte0_e32 v104, v104
	v_cvt_f32_ubyte0_e32 v105, v105
	v_mul_f32_e32 v104, v204, v104
	v_mul_f32_e32 v105, v204, v105
	v_exp_f32_e32 v104, v104
	v_exp_f32_e32 v105, v105
	s_nop 0
	v_pk_mul_f32 v[118:119], v[104:105], v[106:107]
	v_cvt_pk_bf16_f32 v104, v110, v111
	v_add_u32_e32 v110, 0xfc00, v108
	v_cvt_pk_bf16_f32 v105, v114, v115
	ds_read_b64_tr_b16 v[108:109], v108 offset:64512
	ds_read_b64_tr_b16 v[110:111], v110 offset:4608
	v_exp_f32_e32 v114, v113
	v_sub_u32_e32 v113, 30, v184
	v_cvt_f32_ubyte0_e32 v113, v113
	v_mul_f32_e32 v113, v204, v113
	v_exp_f32_e32 v115, v113
	v_cvt_pk_bf16_f32 v106, v116, v117
	s_waitcnt lgkmcnt(1)
	v_lshlrev_b32_e32 v116, 16, v108
	v_and_b32_e32 v117, 0xffff0000, v108
	v_sub_u32_e32 v108, 29, v184
	v_cvt_f32_ubyte0_e32 v108, v108
	v_mul_f32_e32 v108, v204, v108
	v_pk_mul_f32 v[114:115], v[114:115], v[116:117]
	v_exp_f32_e32 v116, v108
	v_sub_u32_e32 v108, 28, v184
	v_cvt_f32_ubyte0_e32 v108, v108
	v_mul_f32_e32 v108, v204, v108
	v_exp_f32_e32 v117, v108
	v_lshlrev_b32_e32 v108, 16, v109
	v_and_b32_e32 v109, 0xffff0000, v109
	v_cvt_pk_bf16_f32 v107, v118, v119
	v_pk_mul_f32 v[116:117], v[116:117], v[108:109]
	v_xor_b32_e32 v108, 15, v184
	v_sub_u32_e32 v109, 14, v184
	v_cvt_f32_ubyte0_e32 v108, v108
	v_cvt_f32_ubyte0_e32 v109, v109
	v_mul_f32_e32 v108, v204, v108
	v_mul_f32_e32 v109, v204, v109
	v_exp_f32_e32 v108, v108
	v_exp_f32_e32 v109, v109
	s_waitcnt lgkmcnt(0)
; template <bool FWD> __device__ __forceinline__ void state_update_1(LAS unsigned char* lds, f32x4 (&racc)[8], float l2, int w, int g, unsigned qp, unsigned p) {
;     ...
; #pragma unroll
;     for (int nb = 0; nb < 8; ++nb) {
;         racc[nb] = racc[nb] * dec;
; #pragma unroll
;         for (int ks = 0; ks < 4; ++ks) racc[nb] = __builtin_amdgcn_mfma_f32_16x16x32_bf16(vs[ks], trfrag(lds + LK, 32 * ks + 4 * g, 32 * ks + 16 + 4 * g, nb, qp, p), racc[nb], 0, 0, 0);
;     }
	ds_read_b64_tr_b16 v[222:223], v205
	ds_read_b64_tr_b16 v[224:225], v205 offset:4608
	ds_read_b64_tr_b16 v[226:227], v205 offset:9216
	ds_read_b64_tr_b16 v[228:229], v205 offset:13824
	ds_read_b64_tr_b16 v[236:237], v205 offset:18432
	ds_read_b64_tr_b16 v[238:239], v205 offset:23040
	ds_read_b64_tr_b16 v[240:241], v205 offset:27648
	ds_read_b64_tr_b16 v[242:243], v205 offset:32256
	v_lshlrev_b32_e32 v118, 16, v110
	v_and_b32_e32 v119, 0xffff0000, v110
	v_lshlrev_b32_e32 v110, 16, v111
	v_pk_mul_f32 v[118:119], v[108:109], v[118:119]
	v_sub_u32_e32 v108, 13, v184
	v_sub_u32_e32 v109, 12, v184
	v_cvt_f32_ubyte0_e32 v108, v108
	v_cvt_f32_ubyte0_e32 v109, v109
	v_mul_f32_e32 v108, v204, v108
	v_mul_f32_e32 v109, v204, v109
	v_exp_f32_e32 v108, v108
	v_exp_f32_e32 v109, v109
	v_and_b32_e32 v111, 0xffff0000, v111
	v_pk_mul_f32 v[22:23], v[22:23], v[112:113] op_sel_hi:[1,0]
	v_pk_mul_f32 v[20:21], v[20:21], v[112:113] op_sel_hi:[1,0]
	v_pk_mul_f32 v[120:121], v[108:109], v[110:111]
	v_cvt_pk_bf16_f32 v108, v114, v115
	v_cvt_pk_bf16_f32 v109, v116, v117
	v_cvt_pk_bf16_f32 v110, v118, v119
	s_waitcnt lgkmcnt(6)
	v_mfma_f32_16x16x32_bf16 v[20:23], v[96:99], v[222:225], v[20:23]
	v_cvt_pk_bf16_f32 v111, v120, v121
	v_pk_mul_f32 v[2:3], v[2:3], v[112:113] op_sel_hi:[1,0]
	ds_read_b64_tr_b16 v[222:223], v205 offset:32
	ds_read_b64_tr_b16 v[224:225], v205 offset:4640
	s_waitcnt lgkmcnt(6)
	v_mfma_f32_16x16x32_bf16 v[20:23], v[100:103], v[226:229], v[20:23]
	v_pk_mul_f32 v[0:1], v[0:1], v[112:113] op_sel_hi:[1,0]
	v_pk_mul_f32 v[18:19], v[18:19], v[112:113] op_sel_hi:[1,0]
	ds_read_b64_tr_b16 v[226:227], v205 offset:9248
	ds_read_b64_tr_b16 v[228:229], v205 offset:13856
	s_waitcnt lgkmcnt(6)
	v_mfma_f32_16x16x32_bf16 v[20:23], v[104:107], v[236:239], v[20:23]
	v_pk_mul_f32 v[16:17], v[16:17], v[112:113] op_sel_hi:[1,0]
	ds_read_b64_tr_b16 v[236:237], v205 offset:18464
	ds_read_b64_tr_b16 v[238:239], v205 offset:23072
	s_waitcnt lgkmcnt(6)
	v_mfma_f32_16x16x32_bf16 v[20:23], v[108:111], v[240:243], v[20:23]
	v_pk_mul_f32 v[26:27], v[26:27], v[112:113] op_sel_hi:[1,0]
	v_pk_mul_f32 v[24:25], v[24:25], v[112:113] op_sel_hi:[1,0]
	ds_read_b64_tr_b16 v[240:241], v205 offset:27680
	ds_read_b64_tr_b16 v[242:243], v205 offset:32288
	s_waitcnt lgkmcnt(6)
	v_mfma_f32_16x16x32_bf16 v[0:3], v[96:99], v[222:225], v[0:3]
	v_mul_f32_e64 v6, v6, v112
	v_mul_f32_e64 v7, v7, v112
	v_pk_mul_f32 v[4:5], v[4:5], v[112:113] op_sel_hi:[1,0]
	v_pk_mul_f32 v[10:11], v[10:11], v[112:113] op_sel_hi:[1,0]
	ds_read_b64_tr_b16 v[222:223], v205 offset:64
	ds_read_b64_tr_b16 v[224:225], v205 offset:4672
	s_waitcnt lgkmcnt(6)
	v_mfma_f32_16x16x32_bf16 v[0:3], v[100:103], v[226:229], v[0:3]
	v_pk_mul_f32 v[8:9], v[8:9], v[112:113] op_sel_hi:[1,0]
	v_pk_mul_f32 v[14:15], v[14:15], v[112:113] op_sel_hi:[1,0]
	ds_read_b64_tr_b16 v[226:227], v205 offset:9280
	ds_read_b64_tr_b16 v[228:229], v205 offset:13888
	s_waitcnt lgkmcnt(6)
	v_mfma_f32_16x16x32_bf16 v[0:3], v[104:107], v[236:239], v[0:3]
	v_pk_mul_f32 v[12:13], v[12:13], v[112:113] op_sel_hi:[1,0]
	v_pk_mul_f32 v[30:31], v[30:31], v[112:113] op_sel_hi:[1,0]
	ds_read_b64_tr_b16 v[236:237], v205 offset:18496
	ds_read_b64_tr_b16 v[238:239], v205 offset:23104
	s_waitcnt lgkmcnt(6)
	v_mfma_f32_16x16x32_bf16 v[0:3], v[108:111], v[240:243], v[0:3]
	v_pk_mul_f32 v[28:29], v[28:29], v[112:113] op_sel_hi:[1,0]
	ds_read_b64_tr_b16 v[240:241], v205 offset:27712
	ds_read_b64_tr_b16 v[242:243], v205 offset:32320
	s_waitcnt lgkmcnt(6)
	v_mfma_f32_16x16x32_bf16 v[16:19], v[96:99], v[222:225], v[16:19]
	ds_read_b64_tr_b16 v[222:223], v205 offset:96
	ds_read_b64_tr_b16 v[224:225], v205 offset:4704
	s_waitcnt lgkmcnt(6)
	v_mfma_f32_16x16x32_bf16 v[16:19], v[100:103], v[226:229], v[16:19]
	ds_read_b64_tr_b16 v[226:227], v205 offset:9312
	ds_read_b64_tr_b16 v[228:229], v205 offset:13920
	s_waitcnt lgkmcnt(6)
; template <bool FWD> __device__ __forceinline__ void state_update_1(LAS unsigned char* lds, f32x4 (&racc)[8], float l2, int w, int g, unsigned qp, unsigned p) {
;     ...
; #pragma unroll
;     for (int nb = 0; nb < 8; ++nb) {
;         racc[nb] = racc[nb] * dec;
; #pragma unroll
;         for (int ks = 0; ks < 4; ++ks) racc[nb] = __builtin_amdgcn_mfma_f32_16x16x32_bf16(vs[ks], trfrag(lds + LK, 32 * ks + 4 * g, 32 * ks + 16 + 4 * g, nb, qp, p), racc[nb], 0, 0, 0);
;     }
	v_mfma_f32_16x16x32_bf16 v[16:19], v[104:107], v[236:239], v[16:19]
	ds_read_b64_tr_b16 v[236:237], v205 offset:18528
	ds_read_b64_tr_b16 v[238:239], v205 offset:23136
	s_waitcnt lgkmcnt(6)
	v_mfma_f32_16x16x32_bf16 v[16:19], v[108:111], v[240:243], v[16:19]
	ds_read_b64_tr_b16 v[240:241], v205 offset:27744
	ds_read_b64_tr_b16 v[242:243], v205 offset:32352
	s_waitcnt lgkmcnt(6)
	v_mfma_f32_16x16x32_bf16 v[24:27], v[96:99], v[222:225], v[24:27]
	ds_read_b64_tr_b16 v[222:223], v205 offset:128
	ds_read_b64_tr_b16 v[224:225], v205 offset:4736
	s_waitcnt lgkmcnt(6)
	v_mfma_f32_16x16x32_bf16 v[24:27], v[100:103], v[226:229], v[24:27]
	ds_read_b64_tr_b16 v[226:227], v205 offset:9344
	ds_read_b64_tr_b16 v[228:229], v205 offset:13952
	s_waitcnt lgkmcnt(6)
	v_mfma_f32_16x16x32_bf16 v[24:27], v[104:107], v[236:239], v[24:27]
	ds_read_b64_tr_b16 v[236:237], v205 offset:18560
	ds_read_b64_tr_b16 v[238:239], v205 offset:23168
	s_waitcnt lgkmcnt(6)
	v_mfma_f32_16x16x32_bf16 v[24:27], v[108:111], v[240:243], v[24:27]
	ds_read_b64_tr_b16 v[240:241], v205 offset:27776
	ds_read_b64_tr_b16 v[242:243], v205 offset:32384
	s_waitcnt lgkmcnt(6)
	v_mfma_f32_16x16x32_bf16 v[4:7], v[96:99], v[222:225], v[4:7]
	ds_read_b64_tr_b16 v[222:223], v205 offset:160
	ds_read_b64_tr_b16 v[224:225], v205 offset:4768
	s_waitcnt lgkmcnt(6)
	v_mfma_f32_16x16x32_bf16 v[4:7], v[100:103], v[226:229], v[4:7]
	ds_read_b64_tr_b16 v[226:227], v205 offset:9376
	ds_read_b64_tr_b16 v[228:229], v205 offset:13984
	s_waitcnt lgkmcnt(6)
	v_mfma_f32_16x16x32_bf16 v[4:7], v[104:107], v[236:239], v[4:7]
	ds_read_b64_tr_b16 v[236:237], v205 offset:18592
	ds_read_b64_tr_b16 v[238:239], v205 offset:23200
	s_waitcnt lgkmcnt(6)
	v_mfma_f32_16x16x32_bf16 v[4:7], v[108:111], v[240:243], v[4:7]
	ds_read_b64_tr_b16 v[240:241], v205 offset:27808
	ds_read_b64_tr_b16 v[242:243], v205 offset:32416
	s_waitcnt lgkmcnt(6)
	v_mfma_f32_16x16x32_bf16 v[8:11], v[96:99], v[222:225], v[8:11]
	ds_read_b64_tr_b16 v[222:223], v205 offset:192
	ds_read_b64_tr_b16 v[224:225], v205 offset:4800
	s_waitcnt lgkmcnt(6)
	v_mfma_f32_16x16x32_bf16 v[8:11], v[100:103], v[226:229], v[8:11]
	ds_read_b64_tr_b16 v[226:227], v205 offset:9408
	ds_read_b64_tr_b16 v[228:229], v205 offset:14016
	s_waitcnt lgkmcnt(6)
	v_mfma_f32_16x16x32_bf16 v[8:11], v[104:107], v[236:239], v[8:11]
	ds_read_b64_tr_b16 v[236:237], v205 offset:18624
	ds_read_b64_tr_b16 v[238:239], v205 offset:23232
	s_waitcnt lgkmcnt(6)
	v_mfma_f32_16x16x32_bf16 v[8:11], v[108:111], v[240:243], v[8:11]
	ds_read_b64_tr_b16 v[240:241], v205 offset:27840
	ds_read_b64_tr_b16 v[242:243], v205 offset:32448
	s_waitcnt lgkmcnt(6)
	v_mfma_f32_16x16x32_bf16 v[12:15], v[96:99], v[222:225], v[12:15]
	ds_read_b64_tr_b16 v[222:223], v205 offset:224
	ds_read_b64_tr_b16 v[224:225], v205 offset:4832
	s_waitcnt lgkmcnt(6)
	v_mfma_f32_16x16x32_bf16 v[12:15], v[100:103], v[226:229], v[12:15]
	ds_read_b64_tr_b16 v[226:227], v205 offset:9440
	ds_read_b64_tr_b16 v[228:229], v205 offset:14048
	s_waitcnt lgkmcnt(6)
	v_mfma_f32_16x16x32_bf16 v[12:15], v[104:107], v[236:239], v[12:15]
	ds_read_b64_tr_b16 v[236:237], v205 offset:18656
	ds_read_b64_tr_b16 v[238:239], v205 offset:23264
	s_waitcnt lgkmcnt(6)
	v_mfma_f32_16x16x32_bf16 v[12:15], v[108:111], v[240:243], v[12:15]
	ds_read_b64_tr_b16 v[240:241], v205 offset:27872
	ds_read_b64_tr_b16 v[242:243], v205 offset:32480
	s_waitcnt lgkmcnt(6)
	v_mfma_f32_16x16x32_bf16 v[28:31], v[96:99], v[222:225], v[28:31]
	s_waitcnt lgkmcnt(4)
	v_mfma_f32_16x16x32_bf16 v[28:31], v[100:103], v[226:229], v[28:31]
	s_waitcnt lgkmcnt(2)
	v_mfma_f32_16x16x32_bf16 v[28:31], v[104:107], v[236:239], v[28:31]
	s_waitcnt lgkmcnt(0)
	v_mfma_f32_16x16x32_bf16 v[28:31], v[108:111], v[240:243], v[28:31]
	s_cbranch_scc0 .LBB0_273
